# combine loop: gate-table loads first in the iteration, the TIE loads of the pair after next no longer waited for at the loop top (counted wait 14/12/0 in front of the first gate use)
# baseline (speedup 1.0000x reference)
; DEV int otid() { int t = threadIdx.x; asm volatile("" : "+v"(t)); return t; }
; DEV void phase_combine(const Params& p, int layer, LAS char* lds, bool have_tables = false) {
;     ...
;     const int tid = otid(), lane = tid & 63, gw = blockIdx.x * 8 + (tid >> 6), nw = gridDim.x * 8;
;     const int ntok = layer == 0 ? NTOK : NLAT;
;     const float* mod = (const float*)(ws + WS_MOD) + (size_t)layer * 3 * 6144;
;     const float* modn = (const float*)(ws + WS_MOD) + (size_t)1 * 3 * 6144;
;     const bf16_t* YS = (const bf16_t*)(ws + WS_YS);
;     struct CRow { u32x4 xr[2], ya[2], yb[2]; float w1, w2; };
;     const u32x4* TIE = (const u32x4*)(ws + WS_TIE); const bf16_t* Xr = (const bf16_t*)(ws + WS_X);
;     const int step = nw * 2, t0 = gw * 2;
;     auto issue_rows = [&](int tok, const u32x4& ti, CRow& R) {
;         const int sa = bs[ti[0] >> 16] * MOE_RB + (int)(ti[0] & 0xffffu), sb = bs[ti[1] >> 16] * MOE_RB + (int)(ti[1] & 0xffffu);
;         R.w1 = __uint_as_float(ti[2]); R.w2 = __uint_as_float(ti[3]);
; #pragma unroll
;         for (int j = 0; j < 2; ++j) { const int col = 8 * lane + 512 * j; R.xr[j] = *(const u32x4*)(Xr + (size_t)tok * 1024 + col);
;             R.ya[j] = *(const u32x4*)(YS + (size_t)sa * 1024 + col); R.yb[j] = *(const u32x4*)(YS + (size_t)sb * 1024 + col); } };
;     CRow cur[2], nxt[2]; u32x4 tin[2] = {{0u, 0u, 0u, 0u}, {0u, 0u, 0u, 0u}};
;     if (t0 < ntok) { const u32x4 a0 = TIE[t0], a1 = TIE[t0 + 1]; issue_rows(t0, a0, cur[0]); issue_rows(t0 + 1, a1, cur[1]);
;         if (t0 + step < ntok) { tin[0] = TIE[t0 + step]; tin[1] = TIE[t0 + step + 1]; } }
.LBB0_1485:
	s_or_b64 exec, exec, s[46:47]
	s_mul_i32 s30, s72, 0x4800
	s_lshl_b64 s[2:3], s[30:31], 2
	s_add_u32 s46, s4, s2
	s_addc_u32 s47, s5, s3
	s_add_u32 s48, s4, 0x22000
	s_addc_u32 s49, s5, 0
	v_or_b32_e32 v116, 0x200, v16
	s_add_u32 s2, s6, 0x1000
	s_addc_u32 s3, s7, 0
	v_lshlrev_b32_e32 v178, 2, v16
	v_lshlrev_b32_e32 v2, 2, v116
	v_mov_b32_e32 v3, v179
	v_lshl_add_u64 v[118:119], s[2:3], 0, v[178:179]
	v_lshl_add_u64 v[120:121], s[2:3], 0, v[2:3]
	v_readlane_b32 s2, v253, 53
	v_mov_b64_e32 v[2:3], s[42:43]
	v_lshl_add_u64 v[122:123], s[38:39], 0, v[10:11]
	v_lshl_add_u64 v[124:125], s[20:21], 0, v[10:11]
	v_add_u32_e32 v142, s2, v15
	v_and_b32_e32 v10, 63, v14
	v_mad_i64_i32 v[128:129], s[2:3], v6, s95, v[2:3]
	v_lshlrev_b64 v[2:3], 12, v[6:7]
	v_lshl_or_b32 v2, v10, 5, v2
	v_lshl_add_u64 v[2:3], s[40:41], 0, v[2:3]
	s_mov_b64 s[2:3], 0x1810
	v_lshl_add_u64 v[130:131], v[2:3], 0, s[2:3]
	v_mov_b32_e32 v136, v5
	v_mov_b32_e32 v137, v4
	s_waitcnt vmcnt(1)
	v_mov_b64_e32 v[2:3], v[112:113]
	v_lshlrev_b32_e32 v126, 4, v10
	v_mov_b32_e32 v127, v179
	v_lshl_add_u64 v[132:133], s[4:5], 0, v[8:9]
	s_mov_b64 s[4:5], 0
	v_mov_b64_e32 v[4:5], v[114:115]
	s_waitcnt vmcnt(0)
	s_branch .LBB0_1487

; DEV float bflo(unsigned u) { return __uint_as_float(u << 16); }
; DEV float bfhi(unsigned u) { return __uint_as_float(u & 0xffff0000u); }
; DEV void phase_combine(const Params& p, int layer, LAS char* lds, bool have_tables = false) {
;     ...
;     for (int tok0 = t0; tok0 < ntok; tok0 += step) {
;         const int tn = tok0 + step, tnn = tn + step;
;         u32x4 tif[2] = {tin[0], tin[1]};
;         if (tnn < ntok) { tif[0] = TIE[tnn]; tif[1] = TIE[tnn + 1]; }
;         if (tn < ntok) { issue_rows(tn, tin[0], nxt[0]); issue_rows(tn + 1, tin[1], nxt[1]); }
; #pragma unroll
;         for (int q = 0; q < 2; ++q) { const int tok = tok0 + q;
;             float xv[2][8];
; #pragma unroll
;             for (int j = 0; j < 2; ++j)
; #pragma unroll
;                 for (int e = 0; e < 4; ++e) { xv[j][2 * e] = bflo(cur[q].xr[j][e]); xv[j][2 * e + 1] = bfhi(cur[q].xr[j][e]); }
;             bf16_t* X = (bf16_t*)(ws + WS_X) + (size_t)tok * 1024;
;             const float* g2 = mod + mod_row(tok) * 6144 + 5120;
;             const float w1 = cur[q].w1, w2 = cur[q].w2;
; #pragma unroll
;             for (int j = 0; j < 2; ++j) { const int col = 8 * lane + 512 * j;
;                 const f32x4 ga = *(const f32x4*)(g2 + col), gb = *(const f32x4*)(g2 + col + 4);
.LBB0_1487:
	v_add_u32_e32 v182, -1, v142
	v_min_i32_e32 v182, 0x8000, v182
	v_ashrrev_i32_e32 v182, 14, v182
	v_mul_i32_i24_e32 v182, 0x1800, v182
	v_ashrrev_i32_e32 v183, 31, v182
	v_lshl_add_u64 v[182:183], v[182:183], 2, s[46:47]
	s_mov_b64 s[2:3], 0x15000
	v_lshl_add_u64 v[182:183], v[182:183], 0, s[2:3]
	v_lshl_add_u64 v[184:185], v[182:183], 0, v[178:179]
	global_load_dwordx4 v[166:169], v[184:185], off
	global_load_dwordx4 v[170:173], v[184:185], off offset:16
	v_lshlrev_b32_e32 v188, 2, v116
	v_mov_b32_e32 v189, v179
	v_lshl_add_u64 v[184:185], v[182:183], 0, v[188:189]
	global_load_dwordx4 v[174:177], v[184:185], off
	global_load_dwordx4 v[198:201], v[184:185], off offset:16
	v_min_i32_e32 v182, 0x8000, v142
	v_ashrrev_i32_e32 v182, 14, v182
	v_mul_i32_i24_e32 v182, 0x1800, v182
	v_ashrrev_i32_e32 v183, 31, v182
	v_lshl_add_u64 v[182:183], v[182:183], 2, s[46:47]
	v_lshl_add_u64 v[182:183], v[182:183], 0, s[2:3]
	v_lshl_add_u64 v[184:185], v[182:183], 0, v[178:179]
	global_load_dwordx4 v[202:205], v[184:185], off
	global_load_dwordx4 v[210:213], v[184:185], off offset:16
	v_lshl_add_u64 v[184:185], v[182:183], 0, v[188:189]
	global_load_dwordx4 v[214:217], v[184:185], off
	global_load_dwordx4 v[228:231], v[184:185], off offset:16
	v_add3_u32 v54, s68, v142, -1
	v_ashrrev_i32_e32 v55, 31, v54
	v_cmp_gt_i32_e32 vcc, s12, v54
	v_lshl_add_u64 v[134:135], v[54:55], 4, s[44:45]
	s_and_saveexec_b64 s[6:7], vcc
	s_cselect_b32 s100, 2, 0
	s_cbranch_execz .LBB0_1489
	global_load_dwordx4 v[2:5], v[134:135], off offset:16
.LBB0_1489:
	s_or_b64 exec, exec, s[6:7]
	v_mov_b64_e32 v[54:55], v[96:97]
	v_mov_b64_e32 v[56:57], v[98:99]
	s_and_saveexec_b64 s[6:7], vcc
	s_cbranch_execz .LBB0_1491
	global_load_dwordx4 v[54:57], v[134:135], off
.LBB0_1491:
	s_or_b64 exec, exec, s[6:7]
	v_readlane_b32 s2, v254, 32
	v_readlane_b32 s3, v254, 33
	s_nop 0
	v_add_u32_e32 v134, s2, v142
	v_add_u32_e32 v138, -1, v134
	v_cmp_gt_i32_e32 vcc, s12, v138
	v_cmp_le_i32_e64 s[38:39], s12, v138
	s_and_saveexec_b64 s[6:7], vcc
	s_cselect_b32 s101, 12, 0
	s_add_i32 s100, s100, s101
	s_cbranch_execz .LBB0_1493
	v_bfe_u32 v6, v96, 16, 16
	v_readlane_b32 s2, v253, 58
	v_bfe_u32 v7, v97, 16, 16
	v_and_b32_e32 v8, 0xffff, v96
	v_lshl_add_u32 v6, v6, 2, s2
	ds_read_b32 v6, v6
	v_lshl_add_u32 v7, v7, 2, s2
	ds_read_b32 v7, v7
	v_ashrrev_i32_e32 v139, 31, v138
	v_lshlrev_b64 v[10:11], 11, v[138:139]
	s_waitcnt lgkmcnt(1)
	v_lshl_add_u32 v6, v6, 8, v8
	v_and_b32_e32 v8, 0xffff, v97
	s_waitcnt lgkmcnt(0)
	v_lshl_add_u32 v8, v7, 8, v8
	v_ashrrev_i32_e32 v7, 31, v6
	v_lshlrev_b64 v[6:7], 11, v[6:7]
	v_ashrrev_i32_e32 v9, 31, v8
	v_bfe_u32 v22, v112, 16, 16
	v_lshlrev_b64 v[8:9], 11, v[8:9]
	v_lshl_add_u64 v[10:11], v[122:123], 0, v[10:11]
	v_lshl_add_u64 v[18:19], v[124:125], 0, v[6:7]
	v_lshl_add_u32 v22, v22, 2, s2
	v_bfe_u32 v23, v113, 16, 16
	v_lshl_add_u64 v[26:27], v[124:125], 0, v[8:9]
	global_load_dwordx4 v[6:9], v[10:11], off
	s_nop 0
	global_load_dwordx4 v[10:13], v[10:11], off offset:1024
	s_nop 0
	global_load_dwordx4 v[14:17], v[18:19], off
	s_nop 0
	global_load_dwordx4 v[18:21], v[18:19], off offset:1024
	v_lshl_add_u32 v23, v23, 2, s2
	ds_read_b32 v30, v22
	ds_read_b32 v31, v23
	v_and_b32_e32 v32, 0xffff, v112
	v_ashrrev_i32_e32 v135, 31, v134
	v_lshlrev_b64 v[34:35], 11, v[134:135]
	s_waitcnt lgkmcnt(1)
	v_lshl_add_u32 v30, v30, 8, v32
	v_and_b32_e32 v32, 0xffff, v113
	s_waitcnt lgkmcnt(0)
	v_lshl_add_u32 v32, v31, 8, v32
	v_ashrrev_i32_e32 v31, 31, v30
	v_ashrrev_i32_e32 v33, 31, v32
	v_lshlrev_b64 v[30:31], 11, v[30:31]
	v_lshlrev_b64 v[32:33], 11, v[32:33]
	v_lshl_add_u64 v[34:35], v[122:123], 0, v[34:35]
	v_lshl_add_u64 v[42:43], v[124:125], 0, v[30:31]
	v_lshl_add_u64 v[44:45], v[124:125], 0, v[32:33]
	global_load_dwordx4 v[22:25], v[26:27], off
	s_nop 0
	global_load_dwordx4 v[26:29], v[26:27], off offset:1024
	s_nop 0
	global_load_dwordx4 v[30:33], v[34:35], off
	s_nop 0
	global_load_dwordx4 v[34:37], v[34:35], off offset:1024
	s_nop 0
	global_load_dwordx4 v[38:41], v[42:43], off
	global_load_dwordx4 v[46:49], v[42:43], off offset:1024
	global_load_dwordx4 v[50:53], v[44:45], off
	s_nop 0
	global_load_dwordx4 v[42:45], v[44:45], off offset:1024
	v_mov_b32_e32 v117, v115
	v_mov_b32_e32 v139, v114
	v_mov_b32_e32 v140, v98
	v_mov_b32_e32 v141, v99
.LBB0_1493:
	s_or_b64 exec, exec, s[6:7]
	v_add_u32_e32 v96, -1, v142
	v_min_i32_e32 v96, 0x8000, v96
	v_ashrrev_i32_e32 v96, 14, v96
	v_mul_i32_i24_e32 v112, 0x1800, v96
	v_ashrrev_i32_e32 v113, 31, v112
	v_lshl_add_u64 v[96:97], v[112:113], 2, s[46:47]
	s_mov_b64 s[2:3], 0x15000
	v_lshl_add_u64 v[114:115], v[96:97], 0, s[2:3]
	v_lshl_add_u64 v[96:97], v[114:115], 0, v[178:179]
	v_lshlrev_b32_e32 v150, 16, v104
	v_and_b32_e32 v151, 0xffff0000, v108
	v_pk_mul_f32 v[150:151], v[82:83], v[150:151] op_sel:[1,0] op_sel_hi:[0,1]
	v_lshlrev_b32_e32 v152, 16, v108
	v_and_b32_e32 v153, 0xffff0000, v104
	v_lshlrev_b32_e32 v148, 16, v100
	v_and_b32_e32 v149, 0xffff0000, v100
	v_pk_fma_f32 v[150:151], v[82:83], v[152:153], v[150:151]
	v_lshlrev_b32_e32 v104, 16, v109
	v_lshlrev_b32_e32 v100, 16, v101
	v_and_b32_e32 v101, 0xffff0000, v101
	v_lshlrev_b32_e32 v108, 16, v110
	v_readlane_b32 s2, v254, 55
	v_readlane_b32 s3, v254, 56
	s_mov_b64 s[6:7], -1
	s_and_b64 vcc, exec, s[2:3]
	s_cmp_eq_u32 s100, 14
	s_cbranch_scc1 .Lcmb_w14
	s_cmp_eq_u32 s100, 12
	s_cbranch_scc1 .Lcmb_w12
	s_waitcnt vmcnt(0)
	s_branch .Lcmb_wd
.Lcmb_w14:
	s_waitcnt vmcnt(14)
	s_branch .Lcmb_wd
.Lcmb_w12:
	s_waitcnt vmcnt(12)
